# speedup vs baseline: 1.0447x; 1.0184x over previous
.Lnoprio:
	s_lshl_b64 s[28:29], s[24:25], 16
	s_add_u32 s33, s16, s28
	s_addc_u32 s35, s17, s29
	s_mul_i32 s40, s6, s7
	s_ashr_i32 s7, s6, 31
	s_sub_i32 s41, s24, s40
	s_lshl_b64 s[4:5], s[6:7], 23
	s_add_u32 s4, s8, s4
	s_addc_u32 s5, s9, s5
	s_lshl_b32 s8, s34, 8
	s_lshl_b32 s9, s34, 10
	s_add_u32 s28, s4, s9
	s_addc_u32 s29, s5, 0
	s_lshl_b64 s[4:5], s[6:7], 21
	s_add_u32 s4, s14, s4
	s_addc_u32 s5, s15, s5
	s_lshl_b32 s42, s34, 6
	s_add_u32 s30, s4, s8
	s_addc_u32 s31, s5, 0
	v_and_b32_e32 v171, 15, v162
	s_lshl_b32 s4, s41, 6
	v_mul_u32_u24_e32 v130, s46, v171
	v_add_u32_e32 v130, s48, v130
	v_subrev_u32_e32 v201, 32, v130
	v_max_i32_e32 v130, 0, v201
	v_sub_u32_e32 v131, 0x7ff, v130
	v_cndmask_b32_e64 v130, v131, v130, s[0:1]
	v_bfe_u32 v146, v162, 4, 2
	v_ashrrev_i32_e32 v131, 31, v130
	v_or_b32_e32 v199, v137, v146
	v_lshlrev_b64 v[130:131], 12, v[130:131]
	v_or_b32_e32 v134, 4, v199
	v_lshl_add_u64 v[130:131], s[28:29], 0, v[130:131]
	v_mov_b32_e32 v167, 0
	v_lshlrev_b32_e32 v166, 4, v199
	v_lshl_add_u64 v[132:133], v[130:131], 0, v[166:167]
	v_lshlrev_b32_e32 v166, 4, v134
	v_lshl_add_u64 v[130:131], v[130:131], 0, v[166:167]
	global_load_dwordx4 v[142:145], v[130:131], off
	global_load_dwordx4 v[138:141], v[132:133], off
	v_lshlrev_b32_e32 v164, 2, v199
	v_lshlrev_b32_e32 v170, 2, v134
	v_lshlrev_b32_e32 v134, 8, v171
	s_mov_b32 s4, 0x8400
	v_add3_u32 v203, v134, v164, s4
	v_lshlrev_b32_e32 v134, 1, v1
	v_sub_u32_e32 v135, v134, v171
	v_or_b32_e32 v134, 1, v134
	v_sub_u32_e32 v134, v134, v171
	s_lshl_b32 s4, s34, 4
	v_mul_lo_u32 v206, v134, s46
	v_mul_u32_u24_e32 v134, 6, v1
	s_add_i32 s4, s4, 16
	v_mad_u32_u24 v130, v1, 6, s4
	v_and_b32_e32 v131, 14, v134
	v_and_or_b32 v130, v130, 48, v131
	v_lshlrev_b32_e32 v172, 6, v130
	v_or_b32_e32 v130, 1, v134
	v_add_u32_e32 v130, s4, v130
	v_bitop3_b32 v131, v134, 15, 1 bitop3:0xc8
	v_and_or_b32 v130, v130, 48, v131
	v_lshlrev_b32_e32 v174, 6, v130
	v_mad_u32_u24 v130, v1, 6, 2
	v_add_u32_e32 v131, s4, v130
	v_and_b32_e32 v132, 14, v130
	v_and_or_b32 v131, v131, 48, v132
	v_lshlrev_b32_e32 v176, 6, v131
	v_mad_u32_u24 v131, v1, 6, 3
	v_and_b32_e32 v136, 63, v162
	v_add_u32_e32 v132, s4, v131
	v_and_b32_e32 v133, 15, v131
	v_lshlrev_b32_e32 v166, 2, v136
	v_and_or_b32 v132, v132, 48, v133
	v_mul_lo_u32 v204, v135, s46
	v_lshl_or_b32 v135, v1, 9, v166
	v_lshlrev_b32_e32 v178, 6, v132
	v_mad_u32_u24 v132, v1, 6, 4
	v_add_u32_e32 v205, 0x8400, v135
	v_add_u32_e32 v133, s4, v132
	v_and_b32_e32 v135, 14, v132
	v_and_or_b32 v133, v133, 48, v135
	s_add_i32 s34, s34, 1
	v_lshrrev_b32_e32 v134, 4, v134
	v_lshl_add_u32 v184, v1, 7, s9
	v_lshlrev_b32_e32 v180, 6, v133
	v_mad_u32_u24 v133, v1, 6, 5
	v_add_lshl_u32 v134, s34, v134, 6
	v_mul_u32_u24_e32 v1, 24, v1
	v_and_b32_e32 v134, 0xc0, v134
	v_and_b32_e32 v1, 56, v1
	v_or3_b32 v183, v1, v134, v146
	v_lshrrev_b32_e32 v1, 4, v130
	v_add_lshl_u32 v1, s34, v1, 6
	v_lshlrev_b32_e32 v130, 2, v130
	v_and_b32_e32 v1, 0xc0, v1
	v_and_b32_e32 v130, 56, v130
	v_or3_b32 v185, v130, v1, v146
	v_lshrrev_b32_e32 v1, 4, v131
	v_add_lshl_u32 v1, s34, v1, 6
	v_lshlrev_b32_e32 v130, 2, v131
	v_and_b32_e32 v1, 0xc0, v1
	v_and_b32_e32 v130, 60, v130
	v_or3_b32 v192, v130, v1, v146
	v_lshrrev_b32_e32 v1, 4, v132
	v_add_lshl_u32 v1, s34, v1, 6
	v_lshlrev_b32_e32 v130, 2, v132
	v_and_b32_e32 v1, 0xc0, v1
	v_and_b32_e32 v130, 56, v130
	v_or3_b32 v193, v130, v1, v146
	v_lshrrev_b32_e32 v1, 4, v133
	v_add_u32_e32 v135, s4, v133
	v_and_b32_e32 v137, 15, v133
	v_add_lshl_u32 v1, s34, v1, 6
	v_lshlrev_b32_e32 v130, 2, v133
	v_and_or_b32 v135, v135, 48, v137
	v_and_b32_e32 v1, 0xc0, v1
	v_and_b32_e32 v130, 60, v130
	v_lshlrev_b32_e32 v182, 6, v135
	v_or3_b32 v194, v130, v1, v146
	v_lshlrev_b32_e32 v168, 3, v136
	s_waitcnt vmcnt(1)
	v_mov_b64_e32 v[130:131], v[142:143]
	s_waitcnt vmcnt(0)
	v_mov_b64_e32 v[134:135], v[138:139]
	s_mov_b32 s43, 0
	v_lshlrev_b32_e32 v173, 3, v146
	v_and_b32_e32 v200, 48, v162
	v_add_u32_e32 v181, s42, v199
	s_mov_b32 s34, 0x48800000
	s_mov_b32 s36, 0x36800000
	v_mov_b32_e32 v188, v167
	v_mov_b32_e32 v189, v167
	v_mul_u32_u24_e32 v195, 0x210, v171
	v_bfe_u32 v216, v162, 4, 1
	v_bfe_u32 v217, v162, 5, 1
	s_lshr_b32 s4, s42, 6
	s_add_i32 s4, s4, 1
	v_lshlrev_b32_e32 v218, 3, v171
	v_lshrrev_b32_e32 v219, 6, v162
	v_mad_u32_u24 v219, v219, 6, v217
	v_lshrrev_b32_e32 v220, 4, v219
	v_add_u32_e32 v220, s4, v220
	v_and_b32_e32 v220, 3, v220
	v_and_b32_e32 v221, 15, v219
	v_lshl_add_u32 v222, v220, 4, v221
	v_lshlrev_b32_e32 v223, 6, v222
	v_lshl_add_u32 v223, v216, 1, v223
	v_lshl_add_u32 v223, v171, 2, v223
	v_lshlrev_b32_e32 v228, 3, v223
	v_lshlrev_b32_e32 v223, 2, v222
	v_lshl_add_u32 v223, v216, 1, v223
	v_lshl_add_u32 v231, v223, 1, v195
	v_add_u32_e32 v219, 2, v219
	v_lshrrev_b32_e32 v220, 4, v219
	v_add_u32_e32 v220, s4, v220
	v_and_b32_e32 v220, 3, v220
	v_and_b32_e32 v221, 15, v219
	v_lshl_add_u32 v222, v220, 4, v221
	v_lshlrev_b32_e32 v223, 6, v222
	v_lshl_add_u32 v223, v216, 1, v223
	v_lshl_add_u32 v223, v171, 2, v223
	v_lshlrev_b32_e32 v229, 3, v223
	v_lshlrev_b32_e32 v223, 2, v222
	v_lshl_add_u32 v223, v216, 1, v223
	v_lshl_add_u32 v232, v223, 1, v195
	v_add_u32_e32 v219, 2, v219
	v_lshrrev_b32_e32 v220, 4, v219
	v_add_u32_e32 v220, s4, v220
	v_and_b32_e32 v220, 3, v220
	v_and_b32_e32 v221, 15, v219
	v_lshl_add_u32 v222, v220, 4, v221
	v_lshlrev_b32_e32 v223, 6, v222
	v_lshl_add_u32 v223, v216, 1, v223
	v_lshl_add_u32 v223, v171, 2, v223
	v_lshlrev_b32_e32 v230, 3, v223
	v_lshlrev_b32_e32 v223, 2, v222
	v_lshl_add_u32 v223, v216, 1, v223
	v_lshl_add_u32 v233, v223, 1, v195
	v_and_b32_e32 v219, 15, v162
	v_bfe_u32 v220, v162, 4, 2
	v_lshl_add_u32 v219, v219, 2, v220
	v_lshlrev_b32_e32 v219, 3, v219
	v_lshl_add_u32 v234, v184, 3, v219
	v_mov_b32_e32 v207, 1
	v_mov_b32_e32 v202, 0
	v_mov_b32_e32 v198, 0
	v_mov_b32_e32 v197, 0
	v_mov_b32_e32 v196, 0
	v_mov_b32_e32 v179, 0
	v_mov_b32_e32 v177, 0
	v_mov_b32_e32 v175, 0
	v_mov_b32_e32 v1, 0
	v_lshl_add_u64 v[186:187], s[30:31], 0, v[166:167]
	v_mov_b64_e32 v[132:133], v[144:145]
	v_mov_b64_e32 v[136:137], v[140:141]

.LBB1_38:
	global_load_dwordx4 v[140:143], v228, s[52:53] sc1
	global_load_dwordx4 v[144:147], v229, s[52:53] sc1
	global_load_dwordx4 v[148:151], v230, s[52:53] sc1
	s_waitcnt vmcnt(2)
	v_cmp_eq_u32_e32 vcc, s44, v141
	v_cmp_eq_u32_e64 s[6:7], s44, v143
	s_waitcnt vmcnt(1)
	v_cmp_eq_u32_e64 s[8:9], s44, v145
	s_and_b64 s[6:7], vcc, s[6:7]
	v_cmp_eq_u32_e64 s[10:11], s44, v147
	s_and_b64 s[6:7], s[6:7], s[8:9]
	s_waitcnt vmcnt(0)
	v_cmp_eq_u32_e64 s[12:13], s44, v149
	s_and_b64 s[6:7], s[6:7], s[10:11]
	v_cmp_eq_u32_e64 s[14:15], s44, v151
	s_and_b64 s[6:7], s[6:7], s[12:13]
	s_and_b64 s[6:7], s[6:7], s[14:15]
	s_cmp_eq_u64 s[6:7], exec
	s_cbranch_scc1 .Lp8_got
	s_mov_b64 s[6:7], -1
	s_mov_b64 s[8:9], -1
	s_and_b32 s6, s45, 0x3ff
	s_cmpk_eq_i32 s6, 0x3ff
	s_mov_b64 s[6:7], -1
	s_mov_b64 s[10:11], -1
	s_cbranch_scc0 .LBB1_42
	s_mov_b64 s[6:7], 0
	s_cmp_lt_u32 s45, 0x80001
	s_mov_b64 s[10:11], 0
	s_cbranch_scc0 .LBB1_42
	global_load_dword v141, v167, s[22:23] offset:4 sc1
	s_waitcnt vmcnt(0)
	v_cmp_eq_u32_e64 s[10:11], 0, v141

.LBB1_55:
	s_xor_b64 s[10:11], s[10:11], -1
	s_lshl_b64 s[4:5], s[24:25], 15
	s_add_u32 s6, s18, s4
	s_addc_u32 s7, s19, s5
	s_waitcnt vmcnt(0)
	v_lshlrev_b32_e32 v130, 11, v171
	s_mov_b32 s4, 0
	v_mov_b32_e32 v131, 0
	v_lshl_add_u64 v[132:133], s[6:7], 0, v[130:131]
	s_lshl_b32 s6, s42, 3
	s_mov_b32 s7, s4
	v_lshl_add_u64 v[132:133], v[132:133], 0, s[6:7]
	v_lshlrev_b32_e32 v130, 3, v199
	s_cmp_gt_i32 s41, 0
	v_lshl_add_u64 v[132:133], v[132:133], 0, v[130:131]
	v_mov_b32_e32 v135, 1
	v_mov_b32_e32 v134, v188
	s_cselect_b64 s[8:9], -1, 0
	global_store_dwordx2 v[132:133], v[134:135], off sc1
	v_mov_b32_e32 v134, v189
	s_and_b64 s[12:13], s[8:9], exec
	global_store_dwordx2 v[132:133], v[134:135], off offset:32 sc1
	s_cselect_b32 s5, 15, 0
	v_add_co_u32_e32 v133, vcc, -1, v171
	v_mov_b32_e32 v132, s5
	s_or_b64 s[8:9], vcc, s[8:9]
	v_cndmask_b32_e32 v132, v132, v133, vcc
	v_mov_b32_e32 v133, s24
	s_xor_b64 vcc, vcc, s[8:9]
	v_subbrev_co_u32_e32 v134, vcc, 0, v133, vcc
	v_ashrrev_i32_e32 v135, 31, v134
	v_lshlrev_b64 v[136:137], 16, v[134:135]
	v_lshl_add_u64 v[136:137], s[16:17], 0, v[136:137]
	v_ashrrev_i32_e32 v133, 31, v132
	v_lshlrev_b32_e32 v138, 5, v132
	v_mov_b32_e32 v139, 0
	v_lshl_add_u64 v[136:137], v[136:137], 0, v[138:139]
	v_mov_b32_e32 v224, s49
	v_mov_b32_e32 v225, s50
	v_cmp_eq_u32_e32 vcc, 0, v171
	v_mov_b32_e32 v227, 0
	s_nop 0
	v_cndmask_b32_e32 v224, v224, v225, vcc
	v_and_b32_e32 v226, 1, v224
	v_lshlrev_b32_e32 v226, 15, v226
	v_lshl_add_u64 v[136:137], v[136:137], 0, v[226:227]
	v_mov_b32_e32 v139, 0
	v_lshlrev_b32_e32 v208, 5, v171
	v_sub_u32_e32 v138, v228, v208
	v_lshl_add_u64 v[140:141], v[136:137], 0, v[138:139]
	v_sub_u32_e32 v138, v229, v208
	v_lshl_add_u64 v[144:145], v[136:137], 0, v[138:139]
	v_sub_u32_e32 v138, v230, v208
	v_lshl_add_u64 v[148:149], v[136:137], 0, v[138:139]
	v_lshlrev_b64 v[134:135], 15, v[134:135]
	v_lshl_add_u64 v[134:135], s[18:19], 0, v[134:135]
	v_lshlrev_b64 v[132:133], 11, v[132:133]
	v_lshl_add_u64 v[132:133], v[134:135], 0, v[132:133]
	v_lshl_add_u64 v[132:133], v[132:133], 0, s[6:7]
	v_lshl_add_u64 v[152:153], v[132:133], 0, v[130:131]
	v_mov_b32_e32 v208, 0
	v_mov_b32_e32 v210, 0
	v_mov_b32_e32 v212, 0
	v_mov_b32_e32 v214, 0
	v_mov_b32_e32 v216, 0
	v_mov_b32_e32 v218, 0
	v_mov_b32_e32 v220, 0
	v_mov_b32_e32 v222, 0
	s_mov_b32 s12, 1
	s_andn2_b64 vcc, exec, s[10:11]
	s_cbranch_vccnz .Lep_check
	s_mov_b32 s7, 0
.Lep_poll:
	global_load_dwordx4 v[208:211], v[140:141], off sc1
	global_load_dwordx4 v[212:215], v[144:145], off sc1
	global_load_dwordx4 v[216:219], v[148:149], off sc1
	global_load_dwordx2 v[220:221], v[152:153], off sc1
	global_load_dwordx2 v[222:223], v[152:153], off offset:32 sc1
	s_waitcnt vmcnt(0)
	v_cmp_eq_u32_e32 vcc, v224, v209
	v_cmp_eq_u32_e64 s[14:15], v224, v211
	v_cmp_eq_u32_e64 s[16:17], v224, v213
	s_and_b64 vcc, vcc, s[14:15]
	v_cmp_eq_u32_e64 s[14:15], v224, v215
	s_and_b64 vcc, vcc, s[16:17]
	v_cmp_eq_u32_e64 s[16:17], v224, v217
	s_and_b64 vcc, vcc, s[14:15]
	v_cmp_eq_u32_e64 s[14:15], v224, v219
	s_and_b64 vcc, vcc, s[16:17]
	v_cmp_eq_u32_e64 s[16:17], 1, v221
	s_and_b64 vcc, vcc, s[14:15]
	v_cmp_eq_u32_e64 s[14:15], 1, v223
	s_and_b64 vcc, vcc, s[16:17]
	s_and_b64 vcc, vcc, s[14:15]
	s_cmp_eq_u64 vcc, exec
	s_cbranch_scc1 .Lep_ok
	s_add_i32 s7, s7, 1
	s_and_b32 s13, s7, 0x3ff
	s_cmp_lg_u32 s13, 0
	s_cbranch_scc1 .Lep_poll
	s_cmp_gt_u32 s7, 0x80000
	s_cbranch_scc1 .Lep_dead
	v_mov_b32_e32 v138, 0
	global_load_dword v139, v138, s[22:23] offset:4 sc1
	s_waitcnt vmcnt(0)
	v_cmp_eq_u32_e64 s[14:15], 0, v139
	s_and_b64 vcc, exec, s[14:15]
	s_cbranch_vccnz .Lep_poll
